# router prologue: the 12 weight/gain loads of a thread all in flight before the LDS fill (was 4 serial round trips)
# speedup vs baseline: 1.0061x; 1.0002x over previous
.LBB0_1618:
	s_mov_b64 s[4:5], 0x800
	s_mov_b64 s[98:99], 0x4000
	global_load_dword v16, v[2:3], off
	global_load_dwordx4 v[8:11], v[4:5], off
	global_load_dwordx4 v[12:15], v[4:5], off offset:-16
	v_lshl_add_u64 v[2:3], v[2:3], 0, s[4:5]
	v_lshl_add_u64 v[4:5], v[4:5], 0, s[98:99]
	global_load_dword v26, v[2:3], off
	global_load_dwordx4 v[18:21], v[4:5], off
	global_load_dwordx4 v[22:25], v[4:5], off offset:-16
	v_lshl_add_u64 v[2:3], v[2:3], 0, s[4:5]
	v_lshl_add_u64 v[4:5], v[4:5], 0, s[98:99]
	global_load_dword v36, v[2:3], off
	global_load_dwordx4 v[28:31], v[4:5], off
	global_load_dwordx4 v[32:35], v[4:5], off offset:-16
	v_lshl_add_u64 v[2:3], v[2:3], 0, s[4:5]
	v_lshl_add_u64 v[4:5], v[4:5], 0, s[98:99]
	global_load_dword v46, v[2:3], off
	global_load_dwordx4 v[38:41], v[4:5], off
	global_load_dwordx4 v[42:45], v[4:5], off offset:-16
	v_and_b32_e32 v7, 0x600, v1
	v_lshrrev_b32_e32 v6, 2, v6
	v_add_u32_e32 v7, v7, v6
	v_lshl_add_u32 v7, v7, 4, 0
	s_waitcnt vmcnt(9)
	v_pk_mul_f32 v[8:9], v[8:9], v[16:17] op_sel_hi:[1,0]
	v_pk_mul_f32 v[10:11], v[10:11], v[16:17] op_sel_hi:[1,0]
	v_pk_mul_f32 v[12:13], v[12:13], v[16:17] op_sel_hi:[1,0]
	v_pk_mul_f32 v[14:15], v[14:15], v[16:17] op_sel_hi:[1,0]
	ds_write_b128 v7, v[12:15]
	ds_write_b128 v7, v[8:11] offset:32768
	s_waitcnt vmcnt(6)
	v_pk_mul_f32 v[18:19], v[18:19], v[26:27] op_sel_hi:[1,0]
	v_pk_mul_f32 v[20:21], v[20:21], v[26:27] op_sel_hi:[1,0]
	v_pk_mul_f32 v[22:23], v[22:23], v[26:27] op_sel_hi:[1,0]
	v_pk_mul_f32 v[24:25], v[24:25], v[26:27] op_sel_hi:[1,0]
	ds_write_b128 v7, v[22:25] offset:2048
	ds_write_b128 v7, v[18:21] offset:34816
	s_waitcnt vmcnt(3)
	v_pk_mul_f32 v[28:29], v[28:29], v[36:37] op_sel_hi:[1,0]
	v_pk_mul_f32 v[30:31], v[30:31], v[36:37] op_sel_hi:[1,0]
	v_pk_mul_f32 v[32:33], v[32:33], v[36:37] op_sel_hi:[1,0]
	v_pk_mul_f32 v[34:35], v[34:35], v[36:37] op_sel_hi:[1,0]
	ds_write_b128 v7, v[32:35] offset:4096
	ds_write_b128 v7, v[28:31] offset:36864
	s_waitcnt vmcnt(0)
	v_pk_mul_f32 v[38:39], v[38:39], v[46:47] op_sel_hi:[1,0]
	v_pk_mul_f32 v[40:41], v[40:41], v[46:47] op_sel_hi:[1,0]
	v_pk_mul_f32 v[42:43], v[42:43], v[46:47] op_sel_hi:[1,0]
	v_pk_mul_f32 v[44:45], v[44:45], v[46:47] op_sel_hi:[1,0]
	ds_write_b128 v7, v[42:45] offset:6144
	ds_write_b128 v7, v[38:41] offset:38912
